# speedup vs baseline: 1.0036x; 1.0036x over previous
.LBB0_18:
	ds_read_b128 v[0:3], v41
	ds_read_b128 v[4:7], v42
	ds_read_b128 v[8:11], v43
	ds_read_b128 v[12:15], v44
	v_add_u32_e32 v45, s6, v136
	v_mad_u64_u32 v[16:17], s[6:7], v45, s9, v[134:135]
	v_lshl_add_u32 v16, v16, 6, v135
	v_add_u32_e32 v137, v16, v34
	v_add_u32_e32 v150, v16, v35
	v_add_u32_e32 v151, v16, v37
	v_add_u32_e32 v152, v16, v38
	v_add_u32_e32 v153, v16, v39
	v_add_u32_e32 v154, v16, v36
	v_add_u32_e32 v16, 0x880, v16
	v_add_u32_e32 v155, v16, v34
	v_add_u32_e32 v156, v16, v35
	v_add_u32_e32 v157, v16, v37
	v_add_u32_e32 v158, v16, v38
	v_add_u32_e32 v159, v16, v39
	v_add_u32_e32 v160, v16, v36
	ds_read_b128 v[46:49], v137 offset:1024
	ds_read_b128 v[122:125], v150 offset:1024
	ds_read_b128 v[126:129], v151 offset:1088
	ds_read_b128 v[130:133], v152 offset:1088
	ds_read_b128 v[138:141], v153 offset:1152
	ds_read_b128 v[142:145], v154 offset:1152
	ds_read_b128 v[146:149], v137 offset:3200
	s_waitcnt lgkmcnt(6)
	v_mfma_f32_32x32x16_f16 v[16:31], v[114:117], v[46:49], v[0:15]
	s_waitcnt lgkmcnt(5)
	v_mfma_f32_32x32x16_f16 v[16:31], v[50:53], v[122:125], v[16:31]
	ds_read_b128 v[46:49], v150 offset:3200
	s_waitcnt lgkmcnt(5)
	v_mfma_f32_32x32x16_f16 v[16:31], v[54:57], v[126:129], v[16:31]
	ds_read_b128 v[122:125], v151 offset:3264
	s_waitcnt lgkmcnt(5)
	v_mfma_f32_32x32x16_f16 v[16:31], v[58:61], v[130:133], v[16:31]
	ds_read_b128 v[126:129], v152 offset:3264
	s_waitcnt lgkmcnt(5)
	v_mfma_f32_32x32x16_f16 v[16:31], v[62:65], v[138:141], v[16:31]
	ds_read_b128 v[130:133], v153 offset:3328
	s_waitcnt lgkmcnt(5)
	v_mfma_f32_32x32x16_f16 v[16:31], v[66:69], v[142:145], v[16:31]
	ds_read_b128 v[138:141], v154 offset:3328
	s_waitcnt lgkmcnt(5)
	v_mfma_f32_32x32x16_f16 v[16:31], v[70:73], v[146:149], v[16:31]
	ds_read_b128 v[142:145], v137 offset:5376
	s_waitcnt lgkmcnt(5)
	v_mfma_f32_32x32x16_f16 v[16:31], v[74:77], v[46:49], v[16:31]
	ds_read_b128 v[146:149], v150 offset:5376
	s_waitcnt lgkmcnt(5)
	v_mfma_f32_32x32x16_f16 v[16:31], v[78:81], v[122:125], v[16:31]
	ds_read_b128 v[46:49], v151 offset:5440
	s_waitcnt lgkmcnt(5)
	v_mfma_f32_32x32x16_f16 v[16:31], v[82:85], v[126:129], v[16:31]
	ds_read_b128 v[122:125], v152 offset:5440
	s_waitcnt lgkmcnt(5)
	v_mfma_f32_32x32x16_f16 v[16:31], v[86:89], v[130:133], v[16:31]
	ds_read_b128 v[126:129], v153 offset:5504
	s_waitcnt lgkmcnt(5)
	v_mfma_f32_32x32x16_f16 v[16:31], v[90:93], v[138:141], v[16:31]
	ds_read_b128 v[130:133], v154 offset:5504
	s_waitcnt lgkmcnt(5)
	v_mfma_f32_32x32x16_f16 v[16:31], v[94:97], v[142:145], v[16:31]
	ds_read_b128 v[138:141], v155 offset:1024
	s_waitcnt lgkmcnt(5)
	v_mfma_f32_32x32x16_f16 v[16:31], v[98:101], v[146:149], v[16:31]
	ds_read_b128 v[142:145], v156 offset:1024
	s_waitcnt lgkmcnt(5)
	v_mfma_f32_32x32x16_f16 v[16:31], v[102:105], v[46:49], v[16:31]
	ds_read_b128 v[146:149], v157 offset:1088
	s_waitcnt lgkmcnt(5)
	v_mfma_f32_32x32x16_f16 v[16:31], v[106:109], v[122:125], v[16:31]
	ds_read_b128 v[46:49], v158 offset:1088
	s_waitcnt lgkmcnt(5)
	v_mfma_f32_32x32x16_f16 v[16:31], v[110:113], v[126:129], v[16:31]
	ds_read_b128 v[122:125], v159 offset:1152
	s_waitcnt lgkmcnt(5)
	v_mfma_f32_32x32x16_f16 v[16:31], v[118:121], v[130:133], v[16:31]
	ds_read_b128 v[126:129], v160 offset:1152
	s_waitcnt lgkmcnt(5)
	v_mfma_f32_32x32x16_f16 v[0:15], v[114:117], v[138:141], v[0:15]
	ds_read_b128 v[130:133], v155 offset:3200
	s_waitcnt lgkmcnt(5)
	v_mfma_f32_32x32x16_f16 v[0:15], v[50:53], v[142:145], v[0:15]
	ds_read_b128 v[138:141], v156 offset:3200
	s_waitcnt lgkmcnt(5)
	v_mfma_f32_32x32x16_f16 v[0:15], v[54:57], v[146:149], v[0:15]
	ds_read_b128 v[142:145], v157 offset:3264
	s_waitcnt lgkmcnt(5)
	v_mfma_f32_32x32x16_f16 v[0:15], v[58:61], v[46:49], v[0:15]
	ds_read_b128 v[146:149], v158 offset:3264
	s_waitcnt lgkmcnt(5)
	v_mfma_f32_32x32x16_f16 v[0:15], v[62:65], v[122:125], v[0:15]
	ds_read_b128 v[46:49], v159 offset:3328
	s_waitcnt lgkmcnt(5)
	v_mfma_f32_32x32x16_f16 v[0:15], v[66:69], v[126:129], v[0:15]
	ds_read_b128 v[122:125], v160 offset:3328
	s_waitcnt lgkmcnt(5)
	v_mfma_f32_32x32x16_f16 v[0:15], v[70:73], v[130:133], v[0:15]
	ds_read_b128 v[126:129], v155 offset:5376
	s_waitcnt lgkmcnt(5)
	v_mfma_f32_32x32x16_f16 v[0:15], v[74:77], v[138:141], v[0:15]
	ds_read_b128 v[130:133], v156 offset:5376
	s_waitcnt lgkmcnt(5)
	v_mfma_f32_32x32x16_f16 v[0:15], v[78:81], v[142:145], v[0:15]
	ds_read_b128 v[138:141], v157 offset:5440
	s_waitcnt lgkmcnt(5)
	v_mfma_f32_32x32x16_f16 v[0:15], v[82:85], v[146:149], v[0:15]
	ds_read_b128 v[142:145], v158 offset:5440
	s_waitcnt lgkmcnt(5)
	v_mfma_f32_32x32x16_f16 v[0:15], v[86:89], v[46:49], v[0:15]
	ds_read_b128 v[146:149], v159 offset:5504
	s_waitcnt lgkmcnt(5)
	v_mfma_f32_32x32x16_f16 v[0:15], v[90:93], v[122:125], v[0:15]
	ds_read_b128 v[46:49], v160 offset:5504
	s_waitcnt lgkmcnt(5)
	v_mfma_f32_32x32x16_f16 v[0:15], v[94:97], v[126:129], v[0:15]
	s_waitcnt lgkmcnt(4)
	v_mfma_f32_32x32x16_f16 v[0:15], v[98:101], v[130:133], v[0:15]
	s_waitcnt lgkmcnt(3)
	v_mfma_f32_32x32x16_f16 v[0:15], v[102:105], v[138:141], v[0:15]
	s_waitcnt lgkmcnt(2)
	v_mfma_f32_32x32x16_f16 v[0:15], v[106:109], v[142:145], v[0:15]
	s_waitcnt lgkmcnt(1)
	v_mfma_f32_32x32x16_f16 v[0:15], v[110:113], v[146:149], v[0:15]
	s_waitcnt lgkmcnt(0)
	v_mfma_f32_32x32x16_f16 v[0:15], v[118:121], v[46:49], v[0:15]
	s_nop 11
	v_cvt_pk_f16_f32 v2, v2, v3
	v_cvt_pk_f16_f32 v3, v4, v5
	v_cvt_pk_f16_f32 v5, v6, v7
	v_cvt_pk_f16_f32 v6, v24, v25
	v_cvt_pk_f16_f32 v7, v8, v9
	v_cvt_pk_f16_f32 v0, v0, v1
	v_cvt_pk_f16_f32 v1, v18, v19
	v_pk_max_f16 v6, v6, v7
	v_cvt_pk_f16_f32 v7, v26, v27
	v_cvt_pk_f16_f32 v8, v10, v11
	v_pk_max_f16 v1, v1, v2
	v_cvt_pk_f16_f32 v2, v20, v21
	v_pk_max_f16 v7, v7, v8
	v_cvt_pk_f16_f32 v8, v28, v29
	v_cvt_pk_f16_f32 v9, v12, v13
	v_cvt_pk_f16_f32 v16, v16, v17
	v_pk_max_f16 v2, v2, v3
	v_cvt_pk_f16_f32 v3, v22, v23
	v_pk_max_f16 v8, v8, v9
	v_cvt_pk_f16_f32 v9, v30, v31
	v_cvt_pk_f16_f32 v12, v14, v15
	v_pk_max_f16 v0, v16, v0
	v_pk_max_f16 v3, v3, v5
	v_pk_max_f16 v9, v9, v12
	v_mov_b32_dpp v16, v0 quad_perm:[1,0,3,2] row_mask:0xf bank_mask:0xf bound_ctrl:1
	v_mov_b32_dpp v17, v1 quad_perm:[1,0,3,2] row_mask:0xf bank_mask:0xf bound_ctrl:1
	v_mov_b32_dpp v4, v2 quad_perm:[1,0,3,2] row_mask:0xf bank_mask:0xf bound_ctrl:1
	v_mov_b32_dpp v5, v3 quad_perm:[1,0,3,2] row_mask:0xf bank_mask:0xf bound_ctrl:1
	v_mov_b32_dpp v18, v6 quad_perm:[1,0,3,2] row_mask:0xf bank_mask:0xf bound_ctrl:1
	v_mov_b32_dpp v10, v7 quad_perm:[1,0,3,2] row_mask:0xf bank_mask:0xf bound_ctrl:1
	v_mov_b32_dpp v11, v8 quad_perm:[1,0,3,2] row_mask:0xf bank_mask:0xf bound_ctrl:1
	v_mov_b32_dpp v12, v9 quad_perm:[1,0,3,2] row_mask:0xf bank_mask:0xf bound_ctrl:1
	s_and_saveexec_b64 s[6:7], s[0:1]
	s_cbranch_execz .LBB0_17
	v_pk_max_f16 v7, v7, v10
	v_pk_max_f16 v8, v8, v11
	v_pk_max_f16 v9, v9, v12
	v_pk_max_f16 v2, v2, v4
	v_pk_max_f16 v3, v3, v5
	v_pk_max_f16 v0, v0, v16
	v_pk_max_f16 v1, v1, v17
	v_pk_max_f16 v6, v6, v18
	v_add_u32_e32 v4, s8, v45
	v_lshl_add_u32 v4, v4, 11, v40
	v_ashrrev_i32_e32 v5, 31, v4
	v_pk_max_f16 v0, v0, 0
	v_pk_max_f16 v1, v1, 0
	v_pk_max_f16 v2, v2, 0
	v_pk_max_f16 v3, v3, 0
	v_lshl_add_u64 v[4:5], v[4:5], 1, v[32:33]
	v_pk_max_f16 v6, v6, 0
	v_pk_max_f16 v7, v7, 0
	v_pk_max_f16 v8, v8, 0
	v_pk_max_f16 v9, v9, 0
	global_store_dwordx4 v[4:5], v[0:3], off sc0 sc1
	global_store_dwordx4 v[4:5], v[6:9], off offset:16 sc0 sc1
	s_branch .LBB0_17
